# k_bhist packing blocks: the three small packing loops (W1p, W2p, bias2) are done by other blocks than the ones already doing 4 serialized trips (block-index xor remap)
# speedup vs baseline: 1.0141x; 1.0141x over previous
.LBB2_20:
	s_and_b64 vcc, exec, s[4:5]
	s_cbranch_vccz .LBB2_66
	s_lshl_b32 s16, s2, 10
	s_add_i32 s2, s16, 0xfffc0000
	v_or_b32_e32 v2, s2, v0
	v_xor_b32_e32 v2, 0xfc00, v2
	s_movk_i32 s2, 0x1000
	v_cmp_gt_i32_e32 vcc, s2, v2
	v_or_b32_e32 v5, s16, v0
	v_xor_b32_e32 v5, 0xfc00, v5
	v_and_b32_e32 v4, 7, v0
	s_and_saveexec_b64 s[2:3], vcc
	s_cbranch_execz .LBB2_29
	s_load_dwordx2 s[6:7], s[0:1], 0x60
	s_load_dwordx2 s[4:5], s[0:1], 0x18
	v_max_i32_e32 v1, 0xffff1000, v2
	v_sub_u32_e32 v1, v1, v5
	v_add_u32_e32 v1, 0x4ffff, v1
	s_mov_b32 s8, 0xffff
	v_cmp_lt_u32_e32 vcc, s8, v1
	s_mov_b64 s[10:11], -1
	v_mov_b32_e32 v6, v2
	s_and_saveexec_b64 s[8:9], vcc
	s_cbranch_execz .LBB2_26
	v_mov_b32_e32 v3, 1
	v_add_u32_sdwa v8, v1, v3 dst_sel:DWORD dst_unused:UNUSED_PAD src0_sel:WORD_1 src1_sel:DWORD
	v_and_b32_e32 v9, 0x1fffe, v8
	v_add_u32_e32 v3, 0x10000, v2
	v_mov_b32_e32 v1, v4
	s_mov_b64 s[10:11], 0
	v_mov_b32_e32 v10, v9
	v_mov_b64_e32 v[6:7], v[2:3]

.LBB2_29:
	s_or_b64 exec, exec, s[2:3]
	v_xor_b32_e32 v2, 0x4000, v2
	v_xor_b32_e32 v5, 0x4000, v5
	s_movk_i32 s2, 0x4000
	v_cmp_gt_i32_e32 vcc, s2, v2
	s_and_saveexec_b64 s[2:3], vcc
	s_cbranch_execz .LBB2_37
	s_waitcnt lgkmcnt(0)
	s_load_dwordx4 s[4:7], s[0:1], 0x20
	v_max_i32_e32 v1, 0xffff4000, v2
	v_sub_u32_e32 v1, v1, v5
	v_add_u32_e32 v1, 0x4ffff, v1
	s_mov_b32 s8, 0xffff
	v_cmp_lt_u32_e32 vcc, s8, v1
	s_mov_b64 s[10:11], -1
	v_mov_b32_e32 v6, v2
	s_and_saveexec_b64 s[8:9], vcc
	s_cbranch_execz .LBB2_34
	v_mov_b32_e32 v3, 1
	v_add_u32_sdwa v8, v1, v3 dst_sel:DWORD dst_unused:UNUSED_PAD src0_sel:WORD_1 src1_sel:DWORD
	v_and_b32_e32 v9, 0x1fffe, v8
	v_add_u32_e32 v3, 0x10000, v2
	v_mov_b32_e32 v1, v4
	s_mov_b64 s[10:11], 0
	v_mov_b32_e32 v10, v9
	v_mov_b64_e32 v[6:7], v[2:3]

.LBB2_37:
	s_or_b64 exec, exec, s[2:3]
	v_xor_b32_e32 v2, 0xbc00, v2
	v_xor_b32_e32 v5, 0xbc00, v5
	s_mov_b32 s2, 0x20000
	v_cmp_gt_i32_e32 vcc, s2, v2
	s_and_saveexec_b64 s[8:9], vcc
	s_cbranch_execz .LBB2_45
	s_load_dwordx2 s[10:11], s[0:1], 0x70
	s_waitcnt lgkmcnt(0)
	s_load_dwordx4 s[4:7], s[0:1], 0x38
	v_max_i32_e32 v1, 0x10000, v2
	v_sub_u32_e32 v1, v1, v5
	v_add_u32_e32 v1, 0x4ffff, v1
	s_mov_b32 s2, 0xffff
	v_cmp_lt_u32_e32 vcc, s2, v1
	s_mov_b64 s[2:3], -1
	v_mov_b32_e32 v6, v2
	s_and_saveexec_b64 s[12:13], vcc
	s_cbranch_execz .LBB2_42
	v_mov_b32_e32 v3, 1
	v_add_u32_sdwa v8, v1, v3 dst_sel:DWORD dst_unused:UNUSED_PAD src0_sel:WORD_1 src1_sel:DWORD
	v_and_b32_e32 v9, 0x1fffe, v8
	v_add_u32_e32 v3, 0x10000, v2
	v_mov_b32_e32 v1, v4
	s_mov_b64 s[14:15], 0
	s_movk_i32 s17, 0x80
	s_movk_i32 s18, 0xff80
	s_waitcnt lgkmcnt(0)
	v_mov_b32_e32 v10, s7
	v_mov_b32_e32 v11, s5
	v_mov_b32_e32 v12, s6
	v_mov_b32_e32 v13, s4
	v_mov_b32_e32 v14, s7
	v_mov_b32_e32 v15, s5
	v_mov_b32_e32 v16, s6
	v_mov_b32_e32 v17, s4
	v_mov_b32_e32 v18, 0xbfb8aa3b
	v_mov_b32_e32 v19, 0x4038aa3b
	v_mov_b32_e32 v20, v9
	v_mov_b64_e32 v[6:7], v[2:3]

.LBB2_58:
	s_or_b64 exec, exec, s[0:1]
	v_xor_b32_e32 v2, 0x4000, v2
	v_xor_b32_e32 v5, 0x4000, v5
	s_movk_i32 s0, 0x200
	v_cmp_gt_i32_e32 vcc, s0, v2
	s_and_saveexec_b64 s[0:1], vcc
	s_cbranch_execz .LBB2_66
	v_max_i32_e32 v0, 0xffff0200, v2
	v_sub_u32_e32 v0, v0, v5
	v_add_u32_e32 v0, 0x4ffff, v0
	s_mov_b32 s0, 0xffff
	v_cmp_lt_u32_e32 vcc, s0, v0
	s_mov_b64 s[8:9], -1
	s_and_saveexec_b64 s[0:1], vcc
	s_cbranch_execz .LBB2_63
	v_mov_b32_e32 v1, 1
	v_add_u32_sdwa v4, v0, v1 dst_sel:DWORD dst_unused:UNUSED_PAD src0_sel:WORD_1 src1_sel:DWORD
	v_and_b32_e32 v5, 0x1fffe, v4
	v_add_u32_e32 v3, 0x10000, v2
	s_mov_b64 s[8:9], 0
	s_movk_i32 s10, 0x100
	v_mov_b32_e32 v6, 0xbfb8aa3b
	v_mov_b32_e32 v7, 0x4038aa3b
	v_mov_b32_e32 v8, v5
	v_mov_b64_e32 v[0:1], v[2:3]
